# hipcc QK schedule kept (no K-read pipelining): dropped vmcnt(0) + 128-cycle spacer after sub-head-0 softmax in both diff loops + dilated stagger
# speedup vs baseline: 1.0169x; 1.0028x over previous
.LBB0_195:
	v_add_u32_e32 v0, s49, v225
	v_add_u32_e32 v6, v0, v227
	ds_read_b128 v[2:5], v6
	s_xor_b64 s[44:45], s[44:45], -1
	s_waitcnt lgkmcnt(0)
	v_mfma_f32_32x32x16_bf16 v[144:159], v[2:5], v[176:179], v[144:159]
	ds_read_b128 v[2:5], v6 offset:8192
	v_add_u32_e32 v6, v0, v228
	s_waitcnt lgkmcnt(0)
	v_mfma_f32_32x32x16_bf16 v[160:175], v[2:5], v[176:179], v[160:175]
	ds_read_b128 v[2:5], v6
	s_waitcnt lgkmcnt(0)
	v_mfma_f32_32x32x16_bf16 v[144:159], v[2:5], v[180:183], v[144:159]
	ds_read_b128 v[2:5], v6 offset:8192
	v_add_u32_e32 v6, v0, v229
	s_waitcnt lgkmcnt(0)
	v_mfma_f32_32x32x16_bf16 v[160:175], v[2:5], v[180:183], v[160:175]
	ds_read_b128 v[2:5], v6
	s_waitcnt lgkmcnt(0)
	v_mfma_f32_32x32x16_bf16 v[144:159], v[2:5], v[184:187], v[144:159]
	ds_read_b128 v[2:5], v6 offset:8192
	v_add_u32_e32 v6, v0, v230
	s_waitcnt lgkmcnt(0)
	v_mfma_f32_32x32x16_bf16 v[160:175], v[2:5], v[184:187], v[160:175]
	ds_read_b128 v[2:5], v6
	s_waitcnt lgkmcnt(0)
	v_mfma_f32_32x32x16_bf16 v[144:159], v[2:5], v[188:191], v[144:159]
	ds_read_b128 v[2:5], v6 offset:8192
	s_waitcnt lgkmcnt(0)
	v_mfma_f32_32x32x16_bf16 v[160:175], v[2:5], v[188:191], v[160:175]
	s_nop 8
	v_exp_f32_e32 v6, v144
	v_exp_f32_e32 v3, v145
	v_exp_f32_e32 v10, v148
	v_exp_f32_e32 v11, v149
	v_exp_f32_e32 v12, v150
	v_exp_f32_e32 v148, v152
	v_exp_f32_e32 v150, v153
	v_exp_f32_e32 v156, v156
	v_exp_f32_e32 v157, v157
	v_exp_f32_e32 v5, v146
	v_exp_f32_e32 v152, v154
	v_exp_f32_e32 v158, v158
	v_exp_f32_e32 v8, v147
	v_exp_f32_e32 v13, v151
	v_exp_f32_e32 v154, v155
	v_exp_f32_e32 v159, v159
	v_exp_f32_e32 v2, v160
	v_exp_f32_e32 v144, v164
	v_exp_f32_e32 v149, v168
	v_exp_f32_e32 v160, v172
	v_exp_f32_e32 v4, v161
	v_exp_f32_e32 v145, v165
	v_exp_f32_e32 v151, v169
	v_exp_f32_e32 v161, v173
	v_add_f32_e32 v14, v6, v3
	v_add_f32_e32 v15, v10, v11
	v_add_f32_e32 v164, v148, v150
	v_add_f32_e32 v165, v156, v157
	v_exp_f32_e32 v7, v162
	v_exp_f32_e32 v146, v166
	v_exp_f32_e32 v153, v170
	v_exp_f32_e32 v162, v174
	v_add_f32_e32 v14, v5, v14
	v_add_f32_e32 v15, v12, v15
	v_add_f32_e32 v164, v152, v164
	v_add_f32_e32 v165, v158, v165
	v_exp_f32_e32 v9, v163
	v_exp_f32_e32 v147, v167
	v_exp_f32_e32 v155, v171
	v_exp_f32_e32 v163, v175
	v_add_f32_e32 v14, v8, v14
	v_add_f32_e32 v15, v13, v15
	v_add_f32_e32 v164, v154, v164
	v_add_f32_e32 v165, v159, v165
	v_add_f32_e32 v14, v2, v14
	v_add_f32_e32 v15, v144, v15
	v_add_f32_e32 v164, v149, v164
	v_add_f32_e32 v165, v160, v165
	v_add_f32_e32 v14, v4, v14
	v_add_f32_e32 v15, v145, v15
	v_add_f32_e32 v164, v151, v164
	v_add_f32_e32 v165, v161, v165
	v_add_f32_e32 v14, v7, v14
	v_add_f32_e32 v15, v146, v15
	v_add_f32_e32 v164, v153, v164
	v_add_f32_e32 v165, v162, v165
	v_add_f32_e32 v14, v9, v14
	v_add_f32_e32 v15, v147, v15
	v_add_f32_e32 v164, v155, v164
	v_add_f32_e32 v165, v163, v165
	v_add_f32_e32 v14, v14, v15
	v_add_f32_e32 v15, v164, v165
	v_add_f32_e32 v14, v14, v15
	v_mov_b32_e32 v15, v14
	v_cvt_pk_bf16_f32 v208, v6, v3
	v_cvt_pk_bf16_f32 v209, v5, v8
	v_cvt_pk_bf16_f32 v210, v10, v11
	v_cvt_pk_bf16_f32 v211, v12, v13
	v_cvt_pk_bf16_f32 v10, v148, v150
	v_cvt_pk_bf16_f32 v11, v152, v154
	v_cvt_pk_bf16_f32 v12, v156, v157
	v_cvt_pk_bf16_f32 v13, v158, v159
	v_cvt_pk_bf16_f32 v6, v2, v4
	v_cvt_pk_bf16_f32 v7, v7, v9
	v_cvt_pk_bf16_f32 v8, v144, v145
	v_cvt_pk_bf16_f32 v9, v146, v147
	v_cvt_pk_bf16_f32 v2, v149, v151
	v_cvt_pk_bf16_f32 v3, v153, v155
	v_cvt_pk_bf16_f32 v4, v160, v161
	v_cvt_pk_bf16_f32 v5, v162, v163
	v_permlane32_swap_b32_e32 v14, v15
	v_permlane32_swap_b32_e32 v208, v210
	v_permlane32_swap_b32_e32 v209, v211
	v_permlane32_swap_b32_e32 v10, v12
	v_permlane32_swap_b32_e32 v11, v13
	v_permlane32_swap_b32_e32 v6, v8
	v_permlane32_swap_b32_e32 v7, v9
	v_permlane32_swap_b32_e32 v2, v4
	v_permlane32_swap_b32_e32 v3, v5
	s_nop 15
	s_nop 15
	v_mov_b32_e32 v160, 0
	s_andn2_b64 vcc, exec, s[44:45]
	v_mov_b32_e32 v161, 0
	v_mov_b32_e32 v162, 0
	v_mov_b32_e32 v163, 0
	v_mov_b32_e32 v164, 0
	v_mov_b32_e32 v165, 0
	v_mov_b32_e32 v166, 0
	v_mov_b32_e32 v167, 0
	v_mov_b32_e32 v168, 0
	v_mov_b32_e32 v169, 0
	v_mov_b32_e32 v170, 0
	v_mov_b32_e32 v171, 0
	v_mov_b32_e32 v172, 0
	v_mov_b32_e32 v173, 0
	v_mov_b32_e32 v174, 0
	v_mov_b32_e32 v175, 0
	v_mov_b32_e32 v144, 0
	v_mov_b32_e32 v145, 0
	v_mov_b32_e32 v146, 0
	v_mov_b32_e32 v147, 0
	v_mov_b32_e32 v148, 0
	v_mov_b32_e32 v149, 0
	v_mov_b32_e32 v150, 0
	v_mov_b32_e32 v151, 0
	v_mov_b32_e32 v152, 0
	v_mov_b32_e32 v153, 0
	v_mov_b32_e32 v154, 0
	v_mov_b32_e32 v155, 0
	v_mov_b32_e32 v156, 0
	v_mov_b32_e32 v157, 0
	v_mov_b32_e32 v158, 0
	v_mov_b32_e32 v159, 0
	s_cbranch_vccnz .LBB0_200
	s_andn2_b64 vcc, exec, s[42:43]
	s_mov_b64 s[42:43], -1
	s_cbranch_vccnz .LBB0_198
	v_add_u32_e32 v144, 0x21780, v212
	v_add_u32_e32 v146, 0x21708, v212
	v_add_u32_e32 v147, 0x21788, v212
	v_add_u32_e32 v148, 0x21720, v212
	v_add_u32_e32 v149, 0x217a0, v212
	v_add_u32_e32 v150, 0x21728, v212
	v_add_u32_e32 v151, 0x217a8, v212
	v_add_u32_e32 v152, 0x21740, v212
	v_add_u32_e32 v153, 0x217c0, v212
	v_add_u32_e32 v154, 0x21748, v212
	v_add_u32_e32 v155, 0x217c8, v212
	v_add_u32_e32 v156, 0x21760, v212
	v_add_u32_e32 v157, 0x217e0, v212
	v_add_u32_e32 v158, 0x21768, v212
	v_add_u32_e32 v159, 0x217e8, v212
	ds_read2_b32 v[160:161], v213 offset1:1
	ds_read2_b32 v[144:145], v144 offset1:1
	ds_read2_b32 v[162:163], v146 offset1:1
	ds_read2_b32 v[146:147], v147 offset1:1
	ds_read2_b32 v[164:165], v148 offset1:1
	ds_read2_b32 v[148:149], v149 offset1:1
	ds_read2_b32 v[166:167], v150 offset1:1
	ds_read2_b32 v[150:151], v151 offset1:1
	ds_read2_b32 v[168:169], v152 offset1:1
	ds_read2_b32 v[152:153], v153 offset1:1
	ds_read2_b32 v[170:171], v154 offset1:1
	ds_read2_b32 v[154:155], v155 offset1:1
	ds_read2_b32 v[172:173], v156 offset1:1
	ds_read2_b32 v[156:157], v157 offset1:1
	ds_read2_b32 v[174:175], v158 offset1:1
	ds_read2_b32 v[158:159], v159 offset1:1
	s_mov_b64 s[42:43], 0

.LBB0_200:
	v_add_u32_e32 v212, v0, v226
	ds_read_b128 v[244:247], v212
	s_waitcnt lgkmcnt(0)
	v_mfma_f32_32x32x16_bf16 v[160:175], v[244:247], v[192:195], v[160:175]
	ds_read_b128 v[244:247], v212 offset:8192
	v_add_u32_e32 v212, v0, v231
	s_waitcnt lgkmcnt(0)
	v_mfma_f32_32x32x16_bf16 v[144:159], v[244:247], v[192:195], v[144:159]
	ds_read_b128 v[244:247], v212
	s_waitcnt lgkmcnt(0)
	v_mfma_f32_32x32x16_bf16 v[160:175], v[244:247], v[196:199], v[160:175]
	ds_read_b128 v[244:247], v212 offset:8192
	v_add_u32_e32 v212, v0, v232
	v_add_u32_e32 v0, v0, v233
	s_waitcnt lgkmcnt(0)
	v_mfma_f32_32x32x16_bf16 v[144:159], v[244:247], v[196:199], v[144:159]
	ds_read_b128 v[244:247], v212
	s_waitcnt lgkmcnt(0)
	v_mfma_f32_32x32x16_bf16 v[160:175], v[244:247], v[200:203], v[160:175]
	ds_read_b128 v[244:247], v212 offset:8192
	s_waitcnt lgkmcnt(0)
	v_mfma_f32_32x32x16_bf16 v[144:159], v[244:247], v[200:203], v[144:159]
	ds_read_b128 v[244:247], v0
	s_waitcnt lgkmcnt(0)
	v_mfma_f32_32x32x16_bf16 v[160:175], v[244:247], v[204:207], v[160:175]
	ds_read_b128 v[244:247], v0 offset:8192
	v_add_f32_e32 v0, v14, v15
	v_add_f32_e32 v235, v235, v0
	s_nop 8
	v_exp_f32_e32 v14, v160
	s_waitcnt lgkmcnt(0)
	v_mfma_f32_32x32x16_bf16 v[144:159], v[244:247], v[204:207], v[144:159]
	v_exp_f32_e32 v160, v161
	v_exp_f32_e32 v164, v164
	v_exp_f32_e32 v15, v168
	v_exp_f32_e32 v161, v169
	v_exp_f32_e32 v162, v162
	v_exp_f32_e32 v220, v163
	v_exp_f32_e32 v166, v166
	s_nop 4
	v_exp_f32_e32 v246, v148
	v_exp_f32_e32 v148, v165
	v_exp_f32_e32 v248, v149
	v_exp_f32_e32 v165, v172
	v_exp_f32_e32 v149, v173
	v_exp_f32_e32 v250, v150
	v_exp_f32_e32 v150, v167
	v_exp_f32_e32 v163, v170
	v_exp_f32_e32 v167, v174
	v_exp_f32_e32 v252, v151
	v_exp_f32_e32 v221, v171
	v_exp_f32_e32 v151, v175
	v_exp_f32_e32 v144, v144
	v_exp_f32_e32 v212, v145
	v_exp_f32_e32 v145, v152
	v_exp_f32_e32 v247, v156
	v_exp_f32_e32 v244, v147
	v_exp_f32_e32 v213, v153
	v_exp_f32_e32 v147, v154
	v_exp_f32_e32 v245, v155
	v_exp_f32_e32 v249, v157
	v_pk_add_f32 v[152:153], v[14:15], v[160:161]
	v_pk_add_f32 v[154:155], v[164:165], v[148:149]
	v_exp_f32_e32 v146, v146
	v_exp_f32_e32 v251, v158
	v_pk_add_f32 v[152:153], v[162:163], v[152:153]
	v_pk_add_f32 v[154:155], v[166:167], v[154:155]
	v_exp_f32_e32 v253, v159
	v_pk_add_f32 v[152:153], v[220:221], v[152:153]
	v_pk_add_f32 v[154:155], v[150:151], v[154:155]
	v_pk_add_f32 v[152:153], v[144:145], v[152:153]
	v_pk_add_f32 v[154:155], v[246:247], v[154:155]
	v_pk_add_f32 v[152:153], v[212:213], v[152:153]
	v_pk_add_f32 v[154:155], v[248:249], v[154:155]
	v_pk_add_f32 v[152:153], v[146:147], v[152:153]
	v_pk_add_f32 v[154:155], v[250:251], v[154:155]
	v_pk_add_f32 v[152:153], v[244:245], v[152:153]
	v_pk_add_f32 v[154:155], v[252:253], v[154:155]
	v_cvt_pk_bf16_f32 v156, v14, v160
	v_pk_add_f32 v[152:153], v[152:153], v[154:155]
	v_cvt_pk_bf16_f32 v157, v162, v220
	v_pk_add_f32 v[152:153], v[152:153], v[152:153] op_sel:[0,1] op_sel_hi:[1,0]
	v_cvt_pk_bf16_f32 v158, v164, v148
	v_mov_b32_e32 v0, v152
	s_nop 1
	v_permlane32_swap_b32_e32 v152, v0
	v_add_f32_e32 v0, v152, v0
	v_cvt_pk_bf16_f32 v159, v166, v150
	v_cvt_pk_bf16_f32 v152, v15, v161
	v_cvt_pk_bf16_f32 v153, v163, v221
	v_cvt_pk_bf16_f32 v154, v165, v149
	v_cvt_pk_bf16_f32 v155, v167, v151
	v_cvt_pk_bf16_f32 v148, v144, v212
	v_cvt_pk_bf16_f32 v149, v146, v244
	v_cvt_pk_bf16_f32 v150, v246, v248
	v_cvt_pk_bf16_f32 v151, v250, v252
	v_cvt_pk_bf16_f32 v144, v145, v213
	v_cvt_pk_bf16_f32 v145, v147, v245
	v_cvt_pk_bf16_f32 v146, v247, v249
	v_cvt_pk_bf16_f32 v147, v251, v253
	v_add_f32_e32 v234, v234, v0
	v_permlane32_swap_b32_e32 v156, v158
	v_permlane32_swap_b32_e32 v157, v159
	v_permlane32_swap_b32_e32 v152, v154
	v_permlane32_swap_b32_e32 v153, v155
	v_permlane32_swap_b32_e32 v148, v150
	v_permlane32_swap_b32_e32 v149, v151
	v_permlane32_swap_b32_e32 v144, v146
	v_permlane32_swap_b32_e32 v145, v147
	s_add_i32 s42, s49, 0x4000
	s_cmpk_lg_u32 s49, 0xc000
	s_cselect_b32 s42, s42, 0
	s_add_i32 s43, s90, 0x4000
	s_cmpk_lg_u32 s90, 0xc000
	s_cselect_b32 s90, s43, 0
	s_add_u32 s40, s40, 0x60000
	s_addc_u32 s41, s41, 0
	s_addk_i32 s71, 0x100
	s_add_i32 s73, s73, 64
	s_add_i32 s86, s86, 1
	s_cmpk_eq_i32 s71, 0x4000
	s_cbranch_scc1 .LBB0_202
	s_mov_b32 s44, s49
	s_mov_b32 s49, s42
	s_cmpk_eq_i32 s71, 0x3f00
	s_mov_b64 s[42:43], -1
	s_cbranch_scc0 .LBB0_191
	s_branch .LBB0_185

.LBB0_205:
	v_add_u32_e32 v219, v212, v226
	ds_read_b128 v[236:239], v219
	s_waitcnt lgkmcnt(0)
	v_mfma_f32_32x32x16_bf16 v[144:159], v[236:239], v[192:195], v[144:159]
	ds_read_b128 v[236:239], v219 offset:8192
	v_add_u32_e32 v219, v212, v231
	s_waitcnt lgkmcnt(0)
	v_mfma_f32_32x32x16_bf16 v[160:175], v[236:239], v[192:195], v[160:175]
	ds_read_b128 v[236:239], v219
	s_waitcnt lgkmcnt(0)
	v_mfma_f32_32x32x16_bf16 v[144:159], v[236:239], v[196:199], v[144:159]
	ds_read_b128 v[236:239], v219 offset:8192
	v_add_u32_e32 v219, v212, v232
	v_add_u32_e32 v212, v212, v233
	s_waitcnt lgkmcnt(0)
	v_mfma_f32_32x32x16_bf16 v[160:175], v[236:239], v[196:199], v[160:175]
	ds_read_b128 v[236:239], v219
	s_waitcnt lgkmcnt(0)
	v_mfma_f32_32x32x16_bf16 v[144:159], v[236:239], v[200:203], v[144:159]
	ds_read_b128 v[236:239], v219 offset:8192
	s_waitcnt lgkmcnt(0)
	v_mfma_f32_32x32x16_bf16 v[160:175], v[236:239], v[200:203], v[160:175]
	ds_read_b128 v[236:239], v212
	s_waitcnt lgkmcnt(0)
	v_mfma_f32_32x32x16_bf16 v[144:159], v[236:239], v[204:207], v[144:159]
	ds_read_b128 v[236:239], v212 offset:8192
	v_add_f32_e32 v212, v213, v218
	v_add_f32_e32 v235, v235, v212
	s_nop 8
	v_exp_f32_e32 v212, v144
	s_waitcnt lgkmcnt(0)
	v_mfma_f32_32x32x16_bf16 v[160:175], v[236:239], v[204:207], v[160:175]
	v_exp_f32_e32 v218, v145
	v_exp_f32_e32 v242, v148
	v_exp_f32_e32 v244, v149
	v_exp_f32_e32 v213, v152
	v_exp_f32_e32 v219, v153
	v_exp_f32_e32 v243, v156
	v_exp_f32_e32 v245, v157
	v_exp_f32_e32 v236, v146
	v_exp_f32_e32 v150, v150
	v_exp_f32_e32 v248, v151
	v_exp_f32_e32 v237, v154
	v_exp_f32_e32 v151, v158
	v_exp_f32_e32 v238, v147
	v_exp_f32_e32 v239, v155
	v_exp_f32_e32 v249, v159
	v_exp_f32_e32 v160, v160
	v_exp_f32_e32 v220, v161
	v_exp_f32_e32 v164, v164
	v_exp_f32_e32 v246, v165
	v_exp_f32_e32 v161, v168
	v_exp_f32_e32 v165, v172
	v_exp_f32_e32 v221, v169
	v_exp_f32_e32 v247, v173
	v_pk_add_f32 v[144:145], v[212:213], v[218:219]
	v_pk_add_f32 v[146:147], v[242:243], v[244:245]
	v_exp_f32_e32 v162, v162
	v_exp_f32_e32 v240, v163
	v_exp_f32_e32 v166, v166
	v_exp_f32_e32 v250, v167
	v_exp_f32_e32 v163, v170
	v_exp_f32_e32 v167, v174
	v_pk_add_f32 v[144:145], v[236:237], v[144:145]
	v_pk_add_f32 v[146:147], v[150:151], v[146:147]
	v_exp_f32_e32 v241, v171
	v_exp_f32_e32 v251, v175
	v_pk_add_f32 v[144:145], v[238:239], v[144:145]
	v_pk_add_f32 v[146:147], v[248:249], v[146:147]
	v_pk_add_f32 v[144:145], v[160:161], v[144:145]
	v_pk_add_f32 v[146:147], v[164:165], v[146:147]
	v_pk_add_f32 v[144:145], v[220:221], v[144:145]
	v_pk_add_f32 v[146:147], v[246:247], v[146:147]
	v_pk_add_f32 v[144:145], v[162:163], v[144:145]
	v_pk_add_f32 v[146:147], v[166:167], v[146:147]
	v_pk_add_f32 v[144:145], v[240:241], v[144:145]
	v_pk_add_f32 v[146:147], v[250:251], v[146:147]
	v_cvt_pk_bf16_f32 v148, v213, v219
	v_pk_add_f32 v[144:145], v[144:145], v[146:147]
	v_cvt_pk_bf16_f32 v146, v242, v244
	v_pk_add_f32 v[144:145], v[144:145], v[144:145] op_sel:[0,1] op_sel_hi:[1,0]
	v_cvt_pk_bf16_f32 v147, v150, v248
	v_mov_b32_e32 v145, v144
	s_nop 1
	v_permlane32_swap_b32_e32 v144, v145
	v_add_f32_e32 v144, v144, v145
	v_add_f32_e32 v234, v234, v144
	v_cvt_pk_bf16_f32 v144, v212, v218
	v_cvt_pk_bf16_f32 v145, v236, v238
	v_cvt_pk_bf16_f32 v149, v237, v239
	v_cvt_pk_bf16_f32 v150, v243, v245
	v_cvt_pk_bf16_f32 v151, v151, v249
	v_cvt_pk_bf16_f32 v152, v160, v220
	v_cvt_pk_bf16_f32 v153, v162, v240
	v_cvt_pk_bf16_f32 v154, v164, v246
	v_cvt_pk_bf16_f32 v155, v166, v250
	v_cvt_pk_bf16_f32 v156, v161, v221
	v_cvt_pk_bf16_f32 v157, v163, v241
	v_cvt_pk_bf16_f32 v158, v165, v247
	v_cvt_pk_bf16_f32 v159, v167, v251
	v_permlane32_swap_b32_e32 v144, v146
	v_permlane32_swap_b32_e32 v145, v147
	v_permlane32_swap_b32_e32 v148, v150
	v_permlane32_swap_b32_e32 v149, v151
	v_permlane32_swap_b32_e32 v152, v154
	v_permlane32_swap_b32_e32 v153, v155
	v_permlane32_swap_b32_e32 v156, v158
	v_permlane32_swap_b32_e32 v157, v159
	s_waitcnt lgkmcnt(0)
	v_add_u32_e32 v212, s56, v224
	ds_read_b64_tr_b16 v[160:161], v212 offset:0
	ds_read_b64_tr_b16 v[162:163], v212 offset:0x800
	ds_read_b64_tr_b16 v[164:165], v212 offset:0x200
	ds_read_b64_tr_b16 v[166:167], v212 offset:0xa00
	ds_read_b64_tr_b16 v[168:169], v212 offset:0x400
	ds_read_b64_tr_b16 v[170:171], v212 offset:0xc00
	ds_read_b64_tr_b16 v[172:173], v212 offset:0x600
	ds_read_b64_tr_b16 v[174:175], v212 offset:0xe00
	s_waitcnt lgkmcnt(4)
	s_nop 0
	v_mfma_f32_32x32x16_bf16 v[112:127], v[208:211], v[160:163], v[112:127]
	v_mfma_f32_32x32x16_bf16 v[96:111], v[208:211], v[164:167], v[96:111]
	v_mfma_f32_32x32x16_bf16 v[128:143], v[144:147], v[160:163], v[128:143]
	v_mfma_f32_32x32x16_bf16 v[80:95], v[144:147], v[164:167], v[80:95]
	ds_read_b64_tr_b16 v[160:161], v212 offset:0x1000
	ds_read_b64_tr_b16 v[162:163], v212 offset:0x1800
	ds_read_b64_tr_b16 v[164:165], v212 offset:0x1200
	ds_read_b64_tr_b16 v[166:167], v212 offset:0x1a00
	s_waitcnt lgkmcnt(4)
	v_mfma_f32_32x32x16_bf16 v[64:79], v[208:211], v[168:171], v[64:79]
	v_mfma_f32_32x32x16_bf16 v[48:63], v[208:211], v[172:175], v[48:63]
	v_mfma_f32_32x32x16_bf16 v[32:47], v[144:147], v[168:171], v[32:47]
	v_mfma_f32_32x32x16_bf16 v[16:31], v[144:147], v[172:175], v[16:31]
	ds_read_b64_tr_b16 v[144:145], v212 offset:0x1400
	ds_read_b64_tr_b16 v[146:147], v212 offset:0x1c00
	ds_read_b64_tr_b16 v[168:169], v212 offset:0x1600
	ds_read_b64_tr_b16 v[170:171], v212 offset:0x1e00
	s_waitcnt lgkmcnt(4)
	v_mfma_f32_32x32x16_bf16 v[112:127], v[10:13], v[160:163], v[112:127]
	v_mfma_f32_32x32x16_bf16 v[96:111], v[10:13], v[164:167], v[96:111]
	v_mfma_f32_32x32x16_bf16 v[128:143], v[148:151], v[160:163], v[128:143]
	v_mfma_f32_32x32x16_bf16 v[80:95], v[148:151], v[164:167], v[80:95]
	ds_read_b64_tr_b16 v[160:161], v212 offset:0x2000
	ds_read_b64_tr_b16 v[162:163], v212 offset:0x2800
	ds_read_b64_tr_b16 v[164:165], v212 offset:0x2200
	ds_read_b64_tr_b16 v[166:167], v212 offset:0x2a00
	s_waitcnt lgkmcnt(4)
	v_mfma_f32_32x32x16_bf16 v[64:79], v[10:13], v[144:147], v[64:79]
	v_mfma_f32_32x32x16_bf16 v[48:63], v[10:13], v[168:171], v[48:63]
	v_mfma_f32_32x32x16_bf16 v[32:47], v[148:151], v[144:147], v[32:47]
	v_mfma_f32_32x32x16_bf16 v[16:31], v[148:151], v[168:171], v[16:31]
	ds_read_b64_tr_b16 v[10:11], v212 offset:0x2400
	ds_read_b64_tr_b16 v[12:13], v212 offset:0x2c00
	ds_read_b64_tr_b16 v[144:145], v212 offset:0x2600
	ds_read_b64_tr_b16 v[146:147], v212 offset:0x2e00
	s_waitcnt lgkmcnt(4)
	v_mfma_f32_32x32x16_bf16 v[112:127], v[6:9], v[160:163], v[112:127]
	v_mfma_f32_32x32x16_bf16 v[96:111], v[6:9], v[164:167], v[96:111]
	v_mfma_f32_32x32x16_bf16 v[128:143], v[152:155], v[160:163], v[128:143]
	v_mfma_f32_32x32x16_bf16 v[80:95], v[152:155], v[164:167], v[80:95]
	ds_read_b64_tr_b16 v[148:149], v212 offset:0x3000
	ds_read_b64_tr_b16 v[150:151], v212 offset:0x3800
	ds_read_b64_tr_b16 v[160:161], v212 offset:0x3200
	ds_read_b64_tr_b16 v[162:163], v212 offset:0x3a00
	s_waitcnt lgkmcnt(4)
	v_mfma_f32_32x32x16_bf16 v[64:79], v[6:9], v[10:13], v[64:79]
	v_mfma_f32_32x32x16_bf16 v[48:63], v[6:9], v[144:147], v[48:63]
	v_mfma_f32_32x32x16_bf16 v[32:47], v[152:155], v[10:13], v[32:47]
	v_mfma_f32_32x32x16_bf16 v[16:31], v[152:155], v[144:147], v[16:31]
	ds_read_b64_tr_b16 v[6:7], v212 offset:0x3400
	ds_read_b64_tr_b16 v[8:9], v212 offset:0x3c00
	ds_read_b64_tr_b16 v[10:11], v212 offset:0x3600
	ds_read_b64_tr_b16 v[12:13], v212 offset:0x3e00
	s_waitcnt lgkmcnt(4)
	v_mfma_f32_32x32x16_bf16 v[112:127], v[2:5], v[148:151], v[112:127]
	v_mfma_f32_32x32x16_bf16 v[96:111], v[2:5], v[160:163], v[96:111]
	v_mfma_f32_32x32x16_bf16 v[128:143], v[156:159], v[148:151], v[128:143]
	v_mfma_f32_32x32x16_bf16 v[80:95], v[156:159], v[160:163], v[80:95]
	s_waitcnt lgkmcnt(0)
	v_mfma_f32_32x32x16_bf16 v[64:79], v[2:5], v[6:9], v[64:79]
	v_mfma_f32_32x32x16_bf16 v[48:63], v[2:5], v[10:13], v[48:63]
	v_mfma_f32_32x32x16_bf16 v[32:47], v[156:159], v[6:9], v[32:47]
	v_mfma_f32_32x32x16_bf16 v[16:31], v[156:159], v[10:13], v[16:31]
	s_add_i32 s42, s56, 0x4000
	s_cmpk_lg_u32 s56, 0xc000
	s_cselect_b32 s56, s42, 0
	s_add_i32 s42, s90, 0x4000
	s_cmpk_lg_u32 s90, 0xc000
	s_cselect_b32 s90, s42, 0
	s_add_u32 s40, s40, 0x60000
	s_addc_u32 s41, s41, 0
	s_addk_i32 s73, 0x100
	s_add_i32 s72, s72, 64
	s_add_i32 s71, s71, 1
	s_cmpk_eq_i32 s73, 0x4000
	s_cbranch_scc1 .LBB0_220

.LBB0_215:
	v_add_u32_e32 v212, s56, v225
	v_add_u32_e32 v6, v212, v227
	ds_read_b128 v[2:5], v6
	s_xor_b64 s[44:45], s[44:45], -1
	s_waitcnt lgkmcnt(0)
	v_mfma_f32_32x32x16_bf16 v[160:175], v[2:5], v[176:179], v[160:175]
	ds_read_b128 v[2:5], v6 offset:8192
	v_add_u32_e32 v6, v212, v228
	s_waitcnt lgkmcnt(0)
	v_mfma_f32_32x32x16_bf16 v[144:159], v[2:5], v[176:179], v[144:159]
	ds_read_b128 v[2:5], v6
	s_waitcnt lgkmcnt(0)
	v_mfma_f32_32x32x16_bf16 v[160:175], v[2:5], v[180:183], v[160:175]
	ds_read_b128 v[2:5], v6 offset:8192
	v_add_u32_e32 v6, v212, v229
	s_waitcnt lgkmcnt(0)
	v_mfma_f32_32x32x16_bf16 v[144:159], v[2:5], v[180:183], v[144:159]
	ds_read_b128 v[2:5], v6
	s_waitcnt lgkmcnt(0)
	v_mfma_f32_32x32x16_bf16 v[160:175], v[2:5], v[184:187], v[160:175]
	ds_read_b128 v[2:5], v6 offset:8192
	v_add_u32_e32 v6, v212, v230
	s_waitcnt lgkmcnt(0)
	v_mfma_f32_32x32x16_bf16 v[144:159], v[2:5], v[184:187], v[144:159]
	ds_read_b128 v[2:5], v6
	s_waitcnt lgkmcnt(0)
	v_mfma_f32_32x32x16_bf16 v[160:175], v[2:5], v[188:191], v[160:175]
	ds_read_b128 v[2:5], v6 offset:8192
	s_waitcnt lgkmcnt(0)
	v_mfma_f32_32x32x16_bf16 v[144:159], v[2:5], v[188:191], v[144:159]
	s_nop 8
	v_exp_f32_e32 v6, v160
	v_exp_f32_e32 v3, v161
	v_exp_f32_e32 v10, v164
	v_exp_f32_e32 v11, v165
	v_exp_f32_e32 v160, v172
	v_exp_f32_e32 v161, v173
	v_exp_f32_e32 v5, v162
	v_exp_f32_e32 v2, v144
	v_exp_f32_e32 v7, v146
	v_exp_f32_e32 v144, v148
	v_exp_f32_e32 v146, v150
	v_exp_f32_e32 v148, v168
	v_exp_f32_e32 v150, v169
	v_exp_f32_e32 v4, v145
	v_exp_f32_e32 v145, v149
	v_exp_f32_e32 v12, v166
	v_exp_f32_e32 v149, v152
	v_exp_f32_e32 v152, v170
	v_exp_f32_e32 v162, v174
	v_exp_f32_e32 v8, v163
	v_exp_f32_e32 v9, v147
	v_exp_f32_e32 v13, v167
	v_exp_f32_e32 v147, v151
	v_exp_f32_e32 v151, v153
	v_exp_f32_e32 v153, v154
	v_exp_f32_e32 v154, v171
	v_exp_f32_e32 v163, v175
	v_exp_f32_e32 v156, v156
	v_exp_f32_e32 v157, v157
	v_add_f32_e32 v164, v6, v3
	v_add_f32_e32 v165, v10, v11
	v_add_f32_e32 v166, v148, v150
	v_add_f32_e32 v167, v160, v161
	v_exp_f32_e32 v158, v158
	v_add_f32_e32 v164, v5, v164
	v_add_f32_e32 v165, v12, v165
	v_add_f32_e32 v166, v152, v166
	v_add_f32_e32 v167, v162, v167
	v_exp_f32_e32 v155, v155
	v_exp_f32_e32 v159, v159
	v_add_f32_e32 v164, v8, v164
	v_add_f32_e32 v165, v13, v165
	v_add_f32_e32 v166, v154, v166
	v_add_f32_e32 v167, v163, v167
	v_add_f32_e32 v164, v2, v164
	v_add_f32_e32 v165, v144, v165
	v_add_f32_e32 v166, v149, v166
	v_add_f32_e32 v167, v156, v167
	v_add_f32_e32 v164, v4, v164
	v_add_f32_e32 v165, v145, v165
	v_add_f32_e32 v166, v151, v166
	v_add_f32_e32 v167, v157, v167
	v_add_f32_e32 v164, v7, v164
	v_add_f32_e32 v165, v146, v165
	v_add_f32_e32 v166, v153, v166
	v_add_f32_e32 v167, v158, v167
	v_add_f32_e32 v164, v9, v164
	v_add_f32_e32 v165, v147, v165
	v_add_f32_e32 v166, v155, v166
	v_add_f32_e32 v167, v159, v167
	v_add_f32_e32 v164, v164, v165
	v_add_f32_e32 v165, v166, v167
	v_add_f32_e32 v213, v164, v165
	v_mov_b32_e32 v218, v213
	v_cvt_pk_bf16_f32 v208, v6, v3
	v_cvt_pk_bf16_f32 v209, v5, v8
	v_cvt_pk_bf16_f32 v210, v10, v11
	v_cvt_pk_bf16_f32 v211, v12, v13
	v_cvt_pk_bf16_f32 v10, v148, v150
	v_cvt_pk_bf16_f32 v11, v152, v154
	v_cvt_pk_bf16_f32 v12, v160, v161
	v_cvt_pk_bf16_f32 v13, v162, v163
	v_cvt_pk_bf16_f32 v6, v2, v4
	v_cvt_pk_bf16_f32 v7, v7, v9
	v_cvt_pk_bf16_f32 v8, v144, v145
	v_cvt_pk_bf16_f32 v9, v146, v147
	v_cvt_pk_bf16_f32 v2, v149, v151
	v_cvt_pk_bf16_f32 v3, v153, v155
	v_cvt_pk_bf16_f32 v4, v156, v157
	v_cvt_pk_bf16_f32 v5, v158, v159
	v_permlane32_swap_b32_e32 v213, v218
	v_permlane32_swap_b32_e32 v208, v210
	v_permlane32_swap_b32_e32 v209, v211
	v_permlane32_swap_b32_e32 v10, v12
	v_permlane32_swap_b32_e32 v11, v13
	v_permlane32_swap_b32_e32 v6, v8
	v_permlane32_swap_b32_e32 v7, v9
	v_permlane32_swap_b32_e32 v2, v4
	v_permlane32_swap_b32_e32 v3, v5
	s_nop 15
	s_nop 15
	v_mov_b32_e32 v160, 0
	s_andn2_b64 vcc, exec, s[44:45]
	v_mov_b32_e32 v161, 0
	v_mov_b32_e32 v162, 0
	v_mov_b32_e32 v163, 0
	v_mov_b32_e32 v164, 0
	v_mov_b32_e32 v165, 0
	v_mov_b32_e32 v166, 0
	v_mov_b32_e32 v167, 0
	v_mov_b32_e32 v168, 0
	v_mov_b32_e32 v169, 0
	v_mov_b32_e32 v170, 0
	v_mov_b32_e32 v171, 0
	v_mov_b32_e32 v172, 0
	v_mov_b32_e32 v173, 0
	v_mov_b32_e32 v174, 0
	v_mov_b32_e32 v175, 0
	v_mov_b32_e32 v144, 0
	v_mov_b32_e32 v145, 0
	v_mov_b32_e32 v146, 0
	v_mov_b32_e32 v147, 0
	v_mov_b32_e32 v148, 0
	v_mov_b32_e32 v149, 0
	v_mov_b32_e32 v150, 0
	v_mov_b32_e32 v151, 0
	v_mov_b32_e32 v152, 0
	v_mov_b32_e32 v153, 0
	v_mov_b32_e32 v154, 0
	v_mov_b32_e32 v155, 0
	v_mov_b32_e32 v156, 0
	v_mov_b32_e32 v157, 0
	v_mov_b32_e32 v158, 0
	v_mov_b32_e32 v159, 0
	s_cbranch_vccnz .LBB0_205
	s_andn2_b64 vcc, exec, s[42:43]
	s_mov_b64 s[42:43], -1
	s_cbranch_vccnz .LBB0_218
	v_add_u32_e32 v146, 0x21780, v219
	v_add_u32_e32 v147, 0x21708, v219
	v_add_u32_e32 v148, 0x21788, v219
	ds_read2_b32 v[144:145], v220 offset1:1
	ds_read2_b32 v[160:161], v146 offset1:1
	ds_read2_b32 v[146:147], v147 offset1:1
	ds_read2_b32 v[162:163], v148 offset1:1
	v_add_u32_e32 v148, 0x21720, v219
	v_add_u32_e32 v150, 0x217a0, v219
	v_add_u32_e32 v151, 0x21728, v219
	v_add_u32_e32 v152, 0x217a8, v219
	ds_read2_b32 v[148:149], v148 offset1:1
	ds_read2_b32 v[164:165], v150 offset1:1
	ds_read2_b32 v[150:151], v151 offset1:1
	ds_read2_b32 v[166:167], v152 offset1:1
	v_add_u32_e32 v152, 0x21740, v219
	v_add_u32_e32 v154, 0x217c0, v219
	v_add_u32_e32 v155, 0x21748, v219
	v_add_u32_e32 v156, 0x217c8, v219
	ds_read2_b32 v[152:153], v152 offset1:1
	ds_read2_b32 v[168:169], v154 offset1:1
	ds_read2_b32 v[154:155], v155 offset1:1
	ds_read2_b32 v[170:171], v156 offset1:1
	v_add_u32_e32 v156, 0x21760, v219
	v_add_u32_e32 v158, 0x217e0, v219
	v_add_u32_e32 v159, 0x21768, v219
	v_add_u32_e32 v174, 0x217e8, v219
	ds_read2_b32 v[156:157], v156 offset1:1
	ds_read2_b32 v[172:173], v158 offset1:1
	ds_read2_b32 v[158:159], v159 offset1:1
	ds_read2_b32 v[174:175], v174 offset1:1
	s_mov_b64 s[42:43], 0
